# c13 + dropped redundant lgkmcnt(0) after MFMA-segment barrier + 8-op row-max tree in attention loops
# speedup vs baseline: 1.2436x; 1.2436x over previous
; #define LAS __attribute__((address_space(3)))
; __device__ __forceinline__ float xhalf_max(float m) { auto rr = __builtin_amdgcn_permlane32_swap(__float_as_uint(m), __float_as_uint(m), false, false); return fmaxf(__uint_as_float(rr[0]), __uint_as_float(rr[1])); }
; template <bool BAND, int OUTMODE>
; __device__ __forceinline__ void compute(LAS unsigned char* lds, const bf16x8 (&qr)[4], int tid, int mq0, int dil, int res, int kt_min, int bias_tab, float sink2,
;                                         bf16* ob, int opitch, float* lsep) {
;     ...
;             for (int i = 0; i < 16; ++i) S[i] = bl[32 * t + (i & 3) + 8 * (i >> 2)];
;         } else {
; #pragma unroll
;             for (int i = 0; i < 16; ++i) S[i] = 0.f;
;         }
; #pragma unroll
;         for (int s = 0; s < 4; ++s) { const bf16x8 kf = *(const LAS bf16x8*)(kb + t * 32 * KSTR + s * 32); S = __builtin_amdgcn_mfma_f32_32x32x16_bf16(kf, qr[s], S, 0, 0, 0); }
;         float m0 = fmaxf(fmaxf(S[0], S[1]), fmaxf(S[2], S[3])), m1 = fmaxf(fmaxf(S[4], S[5]), fmaxf(S[6], S[7])), m2 = fmaxf(fmaxf(S[8], S[9]), fmaxf(S[10], S[11])), m3 = fmaxf(fmaxf(S[12], S[13]), fmaxf(S[14], S[15]));
;         const float mt = xhalf_max(fmaxf(fmaxf(m0, m1), fmaxf(m2, m3)));
;         if (__any(mt > mref + THR)) {
;             const float mnew = fmaxf(mref, mt), f = __builtin_amdgcn_exp2f(mref - mnew);
;             mref = mnew; l *= f;
; #pragma unroll
;             for (int i = 0; i < 16; ++i) { o0[i] *= f; o1[i] *= f; }
;         }
.LBB0_372:
	v_add_u32_e32 v44, 0, v166
	v_add_u32_e32 v36, 0x19800, v44
	v_add_u32_e32 v38, 0x19808, v44
	v_add_u32_e32 v40, 0x19820, v44
	v_add_u32_e32 v42, 0x19828, v44
	ds_read2_b32 v[36:37], v36 offset1:1
	ds_read2_b32 v[38:39], v38 offset1:1
	ds_read2_b32 v[40:41], v40 offset1:1
	ds_read2_b32 v[42:43], v42 offset1:1
	v_add_u32_e32 v45, 0x19840, v44
	v_add_u32_e32 v46, 0x19848, v44
	v_add_u32_e32 v48, 0x19860, v44
	v_add_u32_e32 v50, 0x19868, v44
	v_add_u32_e32 v176, 0, v161
	ds_read_b128 v[168:171], v176
	ds_read2_b32 v[44:45], v45 offset1:1
	ds_read2_b32 v[46:47], v46 offset1:1
	ds_read2_b32 v[48:49], v48 offset1:1
	ds_read2_b32 v[50:51], v50 offset1:1
	ds_read_b128 v[172:175], v176 offset:32
	s_waitcnt vmcnt(18) lgkmcnt(1)
	v_mfma_f32_32x32x16_bf16 v[36:51], v[168:171], v[118:121], v[36:51]
	s_waitcnt vmcnt(17) lgkmcnt(0)
	v_mfma_f32_32x32x16_bf16 v[36:51], v[172:175], v[122:125], v[36:51]
	ds_read_b128 v[168:171], v176 offset:64
	ds_read_b128 v[172:175], v176 offset:96
	s_waitcnt vmcnt(16) lgkmcnt(1)
	v_mfma_f32_32x32x16_bf16 v[36:51], v[168:171], v[126:129], v[36:51]
	s_waitcnt vmcnt(15) lgkmcnt(0)
	v_mfma_f32_32x32x16_bf16 v[36:51], v[172:175], v[130:133], v[36:51]
	s_nop 11
	v_max3_f32 v168, v36, v37, v38
	v_max3_f32 v169, v39, v40, v41
	v_max3_f32 v170, v42, v43, v44
	v_max3_f32 v171, v45, v46, v47
	v_max3_f32 v172, v48, v49, v50
	v_max3_f32 v168, v168, v169, v51
	v_max3_f32 v170, v170, v171, v172
	v_max_f32_e32 v168, v168, v170
	v_mov_b32_e32 v169, v168
	s_nop 1
	v_permlane32_swap_b32_e32 v168, v169
	v_max_f32_e32 v168, v168, v169
	v_add_f32_e32 v169, 0x41000000, v167
	v_cmp_gt_f32_e32 vcc, v168, v169
	s_cbranch_vccz .LBB0_371
	v_max_f32_e32 v168, v168, v168
	v_max_f32_e32 v169, v167, v167
	v_max_f32_e32 v169, v169, v168
	v_sub_f32_e32 v167, v167, v169
	v_exp_f32_e32 v168, v167
	v_mov_b32_e32 v167, v169
	v_pk_mul_f32 v[34:35], v[34:35], v[168:169] op_sel_hi:[1,0]
	v_pk_mul_f32 v[32:33], v[32:33], v[168:169] op_sel_hi:[1,0]
	v_pk_mul_f32 v[30:31], v[30:31], v[168:169] op_sel_hi:[1,0]
	v_pk_mul_f32 v[28:29], v[28:29], v[168:169] op_sel_hi:[1,0]
	v_pk_mul_f32 v[26:27], v[26:27], v[168:169] op_sel_hi:[1,0]
	v_pk_mul_f32 v[24:25], v[24:25], v[168:169] op_sel_hi:[1,0]
	v_pk_mul_f32 v[22:23], v[22:23], v[168:169] op_sel_hi:[1,0]
	v_pk_mul_f32 v[20:21], v[20:21], v[168:169] op_sel_hi:[1,0]
	v_pk_mul_f32 v[18:19], v[18:19], v[168:169] op_sel_hi:[1,0]
	v_pk_mul_f32 v[16:17], v[16:17], v[168:169] op_sel_hi:[1,0]
	v_pk_mul_f32 v[14:15], v[14:15], v[168:169] op_sel_hi:[1,0]
	v_pk_mul_f32 v[12:13], v[12:13], v[168:169] op_sel_hi:[1,0]
	v_pk_mul_f32 v[10:11], v[10:11], v[168:169] op_sel_hi:[1,0]
	v_pk_mul_f32 v[8:9], v[8:9], v[168:169] op_sel_hi:[1,0]
	v_pk_mul_f32 v[6:7], v[6:7], v[168:169] op_sel_hi:[1,0]
	v_pk_mul_f32 v[4:5], v[4:5], v[168:169] op_sel_hi:[1,0]
	v_mul_f32_e32 v137, v137, v168
	s_branch .LBB0_371

; #define LAS __attribute__((address_space(3)))
; __device__ __forceinline__ float xhalf_max(float m) { auto rr = __builtin_amdgcn_permlane32_swap(__float_as_uint(m), __float_as_uint(m), false, false); return fmaxf(__uint_as_float(rr[0]), __uint_as_float(rr[1])); }
; template <bool BAND, int OUTMODE>
; __device__ __forceinline__ void compute(LAS unsigned char* lds, const bf16x8 (&qr)[4], int tid, int mq0, int dil, int res, int kt_min, int bias_tab, float sink2,
;                                         bf16* ob, int opitch, float* lsep) {
;     ...
;             for (int i = 0; i < 16; ++i) S[i] = bl[32 * t + (i & 3) + 8 * (i >> 2)];
;         } else {
; #pragma unroll
;             for (int i = 0; i < 16; ++i) S[i] = 0.f;
;         }
; #pragma unroll
;         for (int s = 0; s < 4; ++s) { const bf16x8 kf = *(const LAS bf16x8*)(kb + t * 32 * KSTR + s * 32); S = __builtin_amdgcn_mfma_f32_32x32x16_bf16(kf, qr[s], S, 0, 0, 0); }
;         float m0 = fmaxf(fmaxf(S[0], S[1]), fmaxf(S[2], S[3])), m1 = fmaxf(fmaxf(S[4], S[5]), fmaxf(S[6], S[7])), m2 = fmaxf(fmaxf(S[8], S[9]), fmaxf(S[10], S[11])), m3 = fmaxf(fmaxf(S[12], S[13]), fmaxf(S[14], S[15]));
;         const float mt = xhalf_max(fmaxf(fmaxf(m0, m1), fmaxf(m2, m3)));
;         if (__any(mt > mref + THR)) {
;             const float mnew = fmaxf(mref, mt), f = __builtin_amdgcn_exp2f(mref - mnew);
;             mref = mnew; l *= f;
; #pragma unroll
;             for (int i = 0; i < 16; ++i) { o0[i] *= f; o1[i] *= f; }
;         }
.LBB0_380:
	v_add_u32_e32 v44, 0, v138
	v_add_u32_e32 v36, 0x19800, v44
	v_add_u32_e32 v38, 0x19808, v44
	v_add_u32_e32 v40, 0x19820, v44
	v_add_u32_e32 v42, 0x19828, v44
	ds_read2_b32 v[36:37], v36 offset1:1
	ds_read2_b32 v[38:39], v38 offset1:1
	ds_read2_b32 v[40:41], v40 offset1:1
	ds_read2_b32 v[42:43], v42 offset1:1
	v_add_u32_e32 v45, 0x19840, v44
	v_add_u32_e32 v46, 0x19848, v44
	v_add_u32_e32 v48, 0x19860, v44
	v_add_u32_e32 v50, 0x19868, v44
	v_add_u32_e32 v174, 0, v137
	ds_read_b128 v[166:169], v174
	ds_read2_b32 v[44:45], v45 offset1:1
	ds_read2_b32 v[46:47], v46 offset1:1
	ds_read2_b32 v[48:49], v48 offset1:1
	ds_read2_b32 v[50:51], v50 offset1:1
	ds_read_b128 v[170:173], v174 offset:32
	s_waitcnt lgkmcnt(1)
	v_mfma_f32_32x32x16_bf16 v[36:51], v[166:169], v[60:63], v[36:51]
	s_waitcnt lgkmcnt(0)
	v_mfma_f32_32x32x16_bf16 v[36:51], v[170:173], v[74:77], v[36:51]
	ds_read_b128 v[166:169], v174 offset:64
	ds_read_b128 v[170:173], v174 offset:96
	s_waitcnt lgkmcnt(1)
	v_mfma_f32_32x32x16_bf16 v[36:51], v[166:169], v[78:81], v[36:51]
	s_waitcnt lgkmcnt(0)
	v_mfma_f32_32x32x16_bf16 v[36:51], v[170:173], v[82:85], v[36:51]
	s_nop 11
	v_max3_f32 v166, v36, v37, v38
	v_max3_f32 v167, v39, v40, v41
	v_max3_f32 v168, v42, v43, v44
	v_max3_f32 v169, v45, v46, v47
	v_max3_f32 v170, v48, v49, v50
	v_max3_f32 v166, v166, v167, v51
	v_max3_f32 v168, v168, v169, v170
	v_max_f32_e32 v166, v166, v168
	v_mov_b32_e32 v167, v166
	s_nop 1
	v_permlane32_swap_b32_e32 v166, v167
	v_max_f32_e32 v166, v166, v167
	v_add_f32_e32 v167, 0x41000000, v139
	v_cmp_gt_f32_e32 vcc, v166, v167
	s_cbranch_vccz .LBB0_379
	v_max_f32_e32 v166, v166, v166
	v_max_f32_e32 v167, v139, v139
	v_max_f32_e32 v167, v167, v166
	v_sub_f32_e32 v139, v139, v167
	v_exp_f32_e32 v166, v139
	v_mov_b32_e32 v139, v167
	v_pk_mul_f32 v[34:35], v[34:35], v[166:167] op_sel_hi:[1,0]
	v_pk_mul_f32 v[32:33], v[32:33], v[166:167] op_sel_hi:[1,0]
	v_pk_mul_f32 v[30:31], v[30:31], v[166:167] op_sel_hi:[1,0]
	v_pk_mul_f32 v[28:29], v[28:29], v[166:167] op_sel_hi:[1,0]
	v_pk_mul_f32 v[26:27], v[26:27], v[166:167] op_sel_hi:[1,0]
	v_pk_mul_f32 v[24:25], v[24:25], v[166:167] op_sel_hi:[1,0]
	v_pk_mul_f32 v[22:23], v[22:23], v[166:167] op_sel_hi:[1,0]
	v_pk_mul_f32 v[20:21], v[20:21], v[166:167] op_sel_hi:[1,0]
	v_pk_mul_f32 v[18:19], v[18:19], v[166:167] op_sel_hi:[1,0]
	v_pk_mul_f32 v[16:17], v[16:17], v[166:167] op_sel_hi:[1,0]
	v_pk_mul_f32 v[14:15], v[14:15], v[166:167] op_sel_hi:[1,0]
	v_pk_mul_f32 v[12:13], v[12:13], v[166:167] op_sel_hi:[1,0]
	v_pk_mul_f32 v[10:11], v[10:11], v[166:167] op_sel_hi:[1,0]
	v_pk_mul_f32 v[8:9], v[8:9], v[166:167] op_sel_hi:[1,0]
	v_pk_mul_f32 v[6:7], v[6:7], v[166:167] op_sel_hi:[1,0]
	v_pk_mul_f32 v[4:5], v[4:5], v[166:167] op_sel_hi:[1,0]
	v_mul_f32_e32 v3, v3, v166
	s_branch .LBB0_379

; #define LAS __attribute__((address_space(3)))
; __device__ __forceinline__ float xhalf_max(float m) { auto rr = __builtin_amdgcn_permlane32_swap(__float_as_uint(m), __float_as_uint(m), false, false); return fmaxf(__uint_as_float(rr[0]), __uint_as_float(rr[1])); }
; template <bool BAND, int OUTMODE>
; __device__ __forceinline__ void compute(LAS unsigned char* lds, const bf16x8 (&qr)[4], int tid, int mq0, int dil, int res, int kt_min, int bias_tab, float sink2,
;                                         bf16* ob, int opitch, float* lsep) {
;     ...
;             for (int i = 0; i < 16; ++i) S[i] = bl[32 * t + (i & 3) + 8 * (i >> 2)];
;         } else {
; #pragma unroll
;             for (int i = 0; i < 16; ++i) S[i] = 0.f;
;         }
; #pragma unroll
;         for (int s = 0; s < 4; ++s) { const bf16x8 kf = *(const LAS bf16x8*)(kb + t * 32 * KSTR + s * 32); S = __builtin_amdgcn_mfma_f32_32x32x16_bf16(kf, qr[s], S, 0, 0, 0); }
;         float m0 = fmaxf(fmaxf(S[0], S[1]), fmaxf(S[2], S[3])), m1 = fmaxf(fmaxf(S[4], S[5]), fmaxf(S[6], S[7])), m2 = fmaxf(fmaxf(S[8], S[9]), fmaxf(S[10], S[11])), m3 = fmaxf(fmaxf(S[12], S[13]), fmaxf(S[14], S[15]));
;         const float mt = xhalf_max(fmaxf(fmaxf(m0, m1), fmaxf(m2, m3)));
;         if (__any(mt > mref + THR)) {
;             const float mnew = fmaxf(mref, mt), f = __builtin_amdgcn_exp2f(mref - mnew);
;             mref = mnew; l *= f;
; #pragma unroll
;             for (int i = 0; i < 16; ++i) { o0[i] *= f; o1[i] *= f; }
;         }
.LBB0_388:
	v_add_u32_e32 v2, 0, v133
	v_add_u32_e32 v4, 0x19800, v2
	v_add_u32_e32 v5, 0x19808, v2
	v_add_u32_e32 v6, 0x19820, v2
	v_add_u32_e32 v7, 0x19828, v2
	ds_read2_b32 v[50:51], v4 offset1:1
	ds_read2_b32 v[52:53], v5 offset1:1
	ds_read2_b32 v[54:55], v6 offset1:1
	ds_read2_b32 v[56:57], v7 offset1:1
	v_add_u32_e32 v8, 0x19840, v2
	v_add_u32_e32 v9, 0x19848, v2
	v_add_u32_e32 v10, 0x19860, v2
	v_add_u32_e32 v12, 0, v132
	v_add_u32_e32 v2, 0x19868, v2
	ds_read_b128 v[4:7], v12
	ds_read2_b32 v[58:59], v8 offset1:1
	ds_read2_b32 v[60:61], v9 offset1:1
	ds_read2_b32 v[62:63], v10 offset1:1
	ds_read2_b32 v[64:65], v2 offset1:1
	ds_read_b128 v[8:11], v12 offset:32
	s_waitcnt lgkmcnt(1)
	v_mfma_f32_32x32x16_bf16 v[50:65], v[4:7], v[86:89], v[50:65]
	s_waitcnt lgkmcnt(0)
	v_mfma_f32_32x32x16_bf16 v[50:65], v[8:11], v[90:93], v[50:65]
	ds_read_b128 v[4:7], v12 offset:64
	ds_read_b128 v[8:11], v12 offset:96
	s_waitcnt lgkmcnt(1)
	v_mfma_f32_32x32x16_bf16 v[50:65], v[4:7], v[94:97], v[50:65]
	s_waitcnt lgkmcnt(0)
	v_mfma_f32_32x32x16_bf16 v[50:65], v[8:11], v[98:101], v[50:65]
	s_nop 11
	v_max3_f32 v2, v50, v51, v52
	v_max3_f32 v4, v53, v54, v55
	v_max3_f32 v5, v56, v57, v58
	v_max3_f32 v6, v59, v60, v61
	v_max3_f32 v7, v62, v63, v64
	v_max3_f32 v2, v2, v4, v65
	v_max3_f32 v5, v5, v6, v7
	v_max_f32_e32 v2, v2, v5
	v_mov_b32_e32 v4, v2
	s_nop 1
	v_permlane32_swap_b32_e32 v2, v4
	v_max_f32_e32 v2, v2, v4
	v_add_f32_e32 v4, 0x41000000, v135
	v_cmp_gt_f32_e32 vcc, v2, v4
	s_cbranch_vccz .LBB0_387
	v_max_f32_e32 v2, v2, v2
	v_max_f32_e32 v4, v135, v135
	v_max_f32_e32 v4, v4, v2
	v_sub_f32_e32 v2, v135, v4
	v_exp_f32_e32 v2, v2
	v_mov_b32_e32 v135, v4
	v_pk_mul_f32 v[48:49], v[48:49], v[2:3] op_sel_hi:[1,0]
	v_pk_mul_f32 v[46:47], v[46:47], v[2:3] op_sel_hi:[1,0]
	v_pk_mul_f32 v[44:45], v[44:45], v[2:3] op_sel_hi:[1,0]
	v_pk_mul_f32 v[42:43], v[42:43], v[2:3] op_sel_hi:[1,0]
	v_pk_mul_f32 v[40:41], v[40:41], v[2:3] op_sel_hi:[1,0]
	v_pk_mul_f32 v[38:39], v[38:39], v[2:3] op_sel_hi:[1,0]
	v_pk_mul_f32 v[36:37], v[36:37], v[2:3] op_sel_hi:[1,0]
	v_pk_mul_f32 v[34:35], v[34:35], v[2:3] op_sel_hi:[1,0]
	v_pk_mul_f32 v[32:33], v[32:33], v[2:3] op_sel_hi:[1,0]
	v_pk_mul_f32 v[30:31], v[30:31], v[2:3] op_sel_hi:[1,0]
	v_pk_mul_f32 v[28:29], v[28:29], v[2:3] op_sel_hi:[1,0]
	v_pk_mul_f32 v[26:27], v[26:27], v[2:3] op_sel_hi:[1,0]
	v_pk_mul_f32 v[24:25], v[24:25], v[2:3] op_sel_hi:[1,0]
	v_pk_mul_f32 v[22:23], v[22:23], v[2:3] op_sel_hi:[1,0]
	v_pk_mul_f32 v[20:21], v[20:21], v[2:3] op_sel_hi:[1,0]
	v_pk_mul_f32 v[18:19], v[18:19], v[2:3] op_sel_hi:[1,0]
	v_mul_f32_e32 v3, v3, v2
	s_branch .LBB0_387

; #define LAS __attribute__((address_space(3)))
; __device__ __forceinline__ float xhalf_max(float m) { auto rr = __builtin_amdgcn_permlane32_swap(__float_as_uint(m), __float_as_uint(m), false, false); return fmaxf(__uint_as_float(rr[0]), __uint_as_float(rr[1])); }
; template <bool BAND, int OUTMODE>
; __device__ __forceinline__ void compute(LAS unsigned char* lds, const bf16x8 (&qr)[4], int tid, int mq0, int dil, int res, int kt_min, int bias_tab, float sink2,
;                                         bf16* ob, int opitch, float* lsep) {
;     ...
;             for (int i = 0; i < 16; ++i) S[i] = 0.f;
;         }
; #pragma unroll
;         for (int s = 0; s < 4; ++s) { const bf16x8 kf = *(const LAS bf16x8*)(kb + t * 32 * KSTR + s * 32); S = __builtin_amdgcn_mfma_f32_32x32x16_bf16(kf, qr[s], S, 0, 0, 0); }
;         float m0 = fmaxf(fmaxf(S[0], S[1]), fmaxf(S[2], S[3])), m1 = fmaxf(fmaxf(S[4], S[5]), fmaxf(S[6], S[7])), m2 = fmaxf(fmaxf(S[8], S[9]), fmaxf(S[10], S[11])), m3 = fmaxf(fmaxf(S[12], S[13]), fmaxf(S[14], S[15]));
;         const float mt = xhalf_max(fmaxf(fmaxf(m0, m1), fmaxf(m2, m3)));
;         if (__any(mt > mref + THR)) {
;             const float mnew = fmaxf(mref, mt), f = __builtin_amdgcn_exp2f(mref - mnew);
;             mref = mnew; l *= f;
; #pragma unroll
;             for (int i = 0; i < 16; ++i) { o0[i] *= f; o1[i] *= f; }
;         }
.LBB0_394:
	v_add_u32_e32 v53, v50, v134
	ds_read_b128 v[34:37], v53
	ds_read_b128 v[54:57], v53 offset:32
	s_waitcnt lgkmcnt(1)
	v_mfma_f32_32x32x16_bf16 v[34:49], v[34:37], v[74:77], 0
	s_waitcnt lgkmcnt(0)
	v_mfma_f32_32x32x16_bf16 v[34:49], v[54:57], v[78:81], v[34:49]
	ds_read_b128 v[54:57], v53 offset:64
	ds_read_b128 v[58:61], v53 offset:96
	s_waitcnt lgkmcnt(1)
	v_mfma_f32_32x32x16_bf16 v[34:49], v[54:57], v[82:85], v[34:49]
	s_waitcnt lgkmcnt(0)
	v_mfma_f32_32x32x16_bf16 v[34:49], v[58:61], v[102:105], v[34:49]
	s_nop 11
	v_max3_f32 v53, v34, v35, v36
	v_max3_f32 v54, v37, v38, v39
	v_max3_f32 v55, v40, v41, v42
	v_max3_f32 v56, v43, v44, v45
	v_max3_f32 v57, v46, v47, v48
	v_max3_f32 v53, v53, v54, v49
	v_max3_f32 v55, v55, v56, v57
	v_max_f32_e32 v53, v53, v55
	v_mov_b32_e32 v54, v53
	s_nop 1
	v_permlane32_swap_b32_e32 v53, v54
	v_max_f32_e32 v53, v53, v54
	v_add_f32_e32 v54, 0x41000000, v52
	v_cmp_gt_f32_e32 vcc, v53, v54
	s_cbranch_vccz .LBB0_393
	v_max_f32_e32 v53, v53, v53
	v_max_f32_e32 v54, v52, v52
	v_max_f32_e32 v53, v54, v53
	v_sub_f32_e32 v52, v52, v53
	v_exp_f32_e32 v52, v52
	s_nop 0
	v_pk_mul_f32 v[32:33], v[32:33], v[52:53] op_sel_hi:[1,0]
	v_pk_mul_f32 v[30:31], v[30:31], v[52:53] op_sel_hi:[1,0]
	v_pk_mul_f32 v[28:29], v[28:29], v[52:53] op_sel_hi:[1,0]
	v_pk_mul_f32 v[26:27], v[26:27], v[52:53] op_sel_hi:[1,0]
	v_pk_mul_f32 v[24:25], v[24:25], v[52:53] op_sel_hi:[1,0]
	v_pk_mul_f32 v[22:23], v[22:23], v[52:53] op_sel_hi:[1,0]
	v_pk_mul_f32 v[20:21], v[20:21], v[52:53] op_sel_hi:[1,0]
	v_pk_mul_f32 v[18:19], v[18:19], v[52:53] op_sel_hi:[1,0]
	v_pk_mul_f32 v[16:17], v[16:17], v[52:53] op_sel_hi:[1,0]
	v_pk_mul_f32 v[14:15], v[14:15], v[52:53] op_sel_hi:[1,0]
	v_pk_mul_f32 v[12:13], v[12:13], v[52:53] op_sel_hi:[1,0]
	v_pk_mul_f32 v[10:11], v[10:11], v[52:53] op_sel_hi:[1,0]
	v_pk_mul_f32 v[8:9], v[8:9], v[52:53] op_sel_hi:[1,0]
	v_pk_mul_f32 v[6:7], v[6:7], v[52:53] op_sel_hi:[1,0]
	v_pk_mul_f32 v[4:5], v[4:5], v[52:53] op_sel_hi:[1,0]
	v_pk_mul_f32 v[2:3], v[2:3], v[52:53] op_sel_hi:[1,0]
	v_mul_f32_e32 v139, v139, v52
	v_mov_b32_e32 v52, v53
	s_branch .LBB0_393

; #define LAS __attribute__((address_space(3)))
; __device__ __forceinline__ float xhalf_max(float m) { auto rr = __builtin_amdgcn_permlane32_swap(__float_as_uint(m), __float_as_uint(m), false, false); return fmaxf(__uint_as_float(rr[0]), __uint_as_float(rr[1])); }
; template <bool BAND, int OUTMODE>
; __device__ __forceinline__ void compute(LAS unsigned char* lds, const bf16x8 (&qr)[4], int tid, int mq0, int dil, int res, int kt_min, int bias_tab, float sink2,
;                                         bf16* ob, int opitch, float* lsep) {
;     ...
;             for (int i = 0; i < 16; ++i) S[i] = bl[32 * t + (i & 3) + 8 * (i >> 2)];
;         } else {
; #pragma unroll
;             for (int i = 0; i < 16; ++i) S[i] = 0.f;
;         }
; #pragma unroll
;         for (int s = 0; s < 4; ++s) { const bf16x8 kf = *(const LAS bf16x8*)(kb + t * 32 * KSTR + s * 32); S = __builtin_amdgcn_mfma_f32_32x32x16_bf16(kf, qr[s], S, 0, 0, 0); }
;         float m0 = fmaxf(fmaxf(S[0], S[1]), fmaxf(S[2], S[3])), m1 = fmaxf(fmaxf(S[4], S[5]), fmaxf(S[6], S[7])), m2 = fmaxf(fmaxf(S[8], S[9]), fmaxf(S[10], S[11])), m3 = fmaxf(fmaxf(S[12], S[13]), fmaxf(S[14], S[15]));
;         const float mt = xhalf_max(fmaxf(fmaxf(m0, m1), fmaxf(m2, m3)));
;         if (__any(mt > mref + THR)) {
;             const float mnew = fmaxf(mref, mt), f = __builtin_amdgcn_exp2f(mref - mnew);
;             mref = mnew; l *= f;
; #pragma unroll
;             for (int i = 0; i < 16; ++i) { o0[i] *= f; o1[i] *= f; }
;         }
.LBB0_941:
	v_add_u32_e32 v44, 0, v167
	v_add_u32_e32 v36, 0x19800, v44
	v_add_u32_e32 v38, 0x19808, v44
	v_add_u32_e32 v40, 0x19820, v44
	v_add_u32_e32 v42, 0x19828, v44
	ds_read2_b32 v[36:37], v36 offset1:1
	ds_read2_b32 v[38:39], v38 offset1:1
	ds_read2_b32 v[40:41], v40 offset1:1
	ds_read2_b32 v[42:43], v42 offset1:1
	v_add_u32_e32 v45, 0x19840, v44
	v_add_u32_e32 v46, 0x19848, v44
	v_add_u32_e32 v48, 0x19860, v44
	v_add_u32_e32 v50, 0x19868, v44
	v_add_u32_e32 v176, 0, v149
	ds_read_b128 v[168:171], v176
	ds_read2_b32 v[44:45], v45 offset1:1
	ds_read2_b32 v[46:47], v46 offset1:1
	ds_read2_b32 v[48:49], v48 offset1:1
	ds_read2_b32 v[50:51], v50 offset1:1
	ds_read_b128 v[172:175], v176 offset:32
	s_waitcnt vmcnt(17) lgkmcnt(1)
	v_mfma_f32_32x32x16_bf16 v[36:51], v[168:171], v[118:121], v[36:51]
	s_waitcnt vmcnt(16) lgkmcnt(0)
	v_mfma_f32_32x32x16_bf16 v[36:51], v[172:175], v[122:125], v[36:51]
	ds_read_b128 v[168:171], v176 offset:64
	ds_read_b128 v[172:175], v176 offset:96
	s_waitcnt vmcnt(15) lgkmcnt(1)
	v_mfma_f32_32x32x16_bf16 v[36:51], v[168:171], v[126:129], v[36:51]
	s_waitcnt vmcnt(14) lgkmcnt(0)
	v_mfma_f32_32x32x16_bf16 v[36:51], v[172:175], v[130:133], v[36:51]
	s_nop 11
	v_max3_f32 v168, v36, v37, v38
	v_max3_f32 v169, v39, v40, v41
	v_max3_f32 v170, v42, v43, v44
	v_max3_f32 v171, v45, v46, v47
	v_max3_f32 v172, v48, v49, v50
	v_max3_f32 v168, v168, v169, v51
	v_max3_f32 v170, v170, v171, v172
	v_max_f32_e32 v168, v168, v170
	v_mov_b32_e32 v169, v168
	s_nop 1
	v_permlane32_swap_b32_e32 v168, v169
	v_max_f32_e32 v168, v168, v169
	v_add_f32_e32 v169, 0x41000000, v165
	v_cmp_gt_f32_e32 vcc, v168, v169
	s_cbranch_vccz .LBB0_940
	v_max_f32_e32 v168, v168, v168
	v_max_f32_e32 v169, v165, v165
	v_max_f32_e32 v169, v169, v168
	v_sub_f32_e32 v165, v165, v169
	v_exp_f32_e32 v168, v165
	v_mov_b32_e32 v165, v169
	v_pk_mul_f32 v[34:35], v[34:35], v[168:169] op_sel_hi:[1,0]
	v_pk_mul_f32 v[32:33], v[32:33], v[168:169] op_sel_hi:[1,0]
	v_pk_mul_f32 v[30:31], v[30:31], v[168:169] op_sel_hi:[1,0]
	v_pk_mul_f32 v[28:29], v[28:29], v[168:169] op_sel_hi:[1,0]
	v_pk_mul_f32 v[26:27], v[26:27], v[168:169] op_sel_hi:[1,0]
	v_pk_mul_f32 v[24:25], v[24:25], v[168:169] op_sel_hi:[1,0]
	v_pk_mul_f32 v[22:23], v[22:23], v[168:169] op_sel_hi:[1,0]
	v_pk_mul_f32 v[20:21], v[20:21], v[168:169] op_sel_hi:[1,0]
	v_pk_mul_f32 v[18:19], v[18:19], v[168:169] op_sel_hi:[1,0]
	v_pk_mul_f32 v[16:17], v[16:17], v[168:169] op_sel_hi:[1,0]
	v_pk_mul_f32 v[14:15], v[14:15], v[168:169] op_sel_hi:[1,0]
	v_pk_mul_f32 v[12:13], v[12:13], v[168:169] op_sel_hi:[1,0]
	v_pk_mul_f32 v[10:11], v[10:11], v[168:169] op_sel_hi:[1,0]
	v_pk_mul_f32 v[8:9], v[8:9], v[168:169] op_sel_hi:[1,0]
	v_pk_mul_f32 v[6:7], v[6:7], v[168:169] op_sel_hi:[1,0]
	v_pk_mul_f32 v[4:5], v[4:5], v[168:169] op_sel_hi:[1,0]
	v_mul_f32_e32 v3, v3, v168
	s_branch .LBB0_940

; #define LAS __attribute__((address_space(3)))
; __device__ __forceinline__ float xhalf_max(float m) { auto rr = __builtin_amdgcn_permlane32_swap(__float_as_uint(m), __float_as_uint(m), false, false); return fmaxf(__uint_as_float(rr[0]), __uint_as_float(rr[1])); }
; template <bool BAND, int OUTMODE>
; __device__ __forceinline__ void compute(LAS unsigned char* lds, const bf16x8 (&qr)[4], int tid, int mq0, int dil, int res, int kt_min, int bias_tab, float sink2,
;                                         bf16* ob, int opitch, float* lsep) {
;     ...
;             for (int i = 0; i < 16; ++i) S[i] = bl[32 * t + (i & 3) + 8 * (i >> 2)];
;         } else {
; #pragma unroll
;             for (int i = 0; i < 16; ++i) S[i] = 0.f;
;         }
; #pragma unroll
;         for (int s = 0; s < 4; ++s) { const bf16x8 kf = *(const LAS bf16x8*)(kb + t * 32 * KSTR + s * 32); S = __builtin_amdgcn_mfma_f32_32x32x16_bf16(kf, qr[s], S, 0, 0, 0); }
;         float m0 = fmaxf(fmaxf(S[0], S[1]), fmaxf(S[2], S[3])), m1 = fmaxf(fmaxf(S[4], S[5]), fmaxf(S[6], S[7])), m2 = fmaxf(fmaxf(S[8], S[9]), fmaxf(S[10], S[11])), m3 = fmaxf(fmaxf(S[12], S[13]), fmaxf(S[14], S[15]));
;         const float mt = xhalf_max(fmaxf(fmaxf(m0, m1), fmaxf(m2, m3)));
;         if (__any(mt > mref + THR)) {
;             const float mnew = fmaxf(mref, mt), f = __builtin_amdgcn_exp2f(mref - mnew);
;             mref = mnew; l *= f;
; #pragma unroll
;             for (int i = 0; i < 16; ++i) { o0[i] *= f; o1[i] *= f; }
;         }
.LBB0_951:
	v_add_u32_e32 v44, 0, v141
	v_add_u32_e32 v36, 0x1a400, v44
	v_add_u32_e32 v38, 0x1a408, v44
	v_add_u32_e32 v40, 0x1a420, v44
	v_add_u32_e32 v42, 0x1a428, v44
	ds_read2_b32 v[36:37], v36 offset1:1
	ds_read2_b32 v[38:39], v38 offset1:1
	ds_read2_b32 v[40:41], v40 offset1:1
	ds_read2_b32 v[42:43], v42 offset1:1
	v_add_u32_e32 v45, 0x1a440, v44
	v_add_u32_e32 v46, 0x1a448, v44
	v_add_u32_e32 v48, 0x1a460, v44
	v_add_u32_e32 v50, 0x1a468, v44
	v_add_u32_e32 v174, 0, v140
	ds_read_b128 v[166:169], v174
	ds_read2_b32 v[44:45], v45 offset1:1
	ds_read2_b32 v[46:47], v46 offset1:1
	ds_read2_b32 v[48:49], v48 offset1:1
	ds_read2_b32 v[50:51], v50 offset1:1
	ds_read_b128 v[170:173], v174 offset:32
	s_waitcnt vmcnt(21) lgkmcnt(1)
	v_mfma_f32_32x32x16_bf16 v[36:51], v[166:169], v[60:63], v[36:51]
	s_waitcnt vmcnt(20) lgkmcnt(0)
	v_mfma_f32_32x32x16_bf16 v[36:51], v[170:173], v[74:77], v[36:51]
	ds_read_b128 v[166:169], v174 offset:64
	ds_read_b128 v[170:173], v174 offset:96
	s_waitcnt vmcnt(19) lgkmcnt(1)
	v_mfma_f32_32x32x16_bf16 v[36:51], v[166:169], v[78:81], v[36:51]
	s_waitcnt vmcnt(18) lgkmcnt(0)
	v_mfma_f32_32x32x16_bf16 v[36:51], v[170:173], v[82:85], v[36:51]
	s_nop 11
	v_max3_f32 v166, v36, v37, v38
	v_max3_f32 v167, v39, v40, v41
	v_max3_f32 v168, v42, v43, v44
	v_max3_f32 v169, v45, v46, v47
	v_max3_f32 v170, v48, v49, v50
	v_max3_f32 v166, v166, v167, v51
	v_max3_f32 v168, v168, v169, v170
	v_max_f32_e32 v166, v166, v168
	v_mov_b32_e32 v167, v166
	s_nop 1
	v_permlane32_swap_b32_e32 v166, v167
	v_max_f32_e32 v166, v166, v167
	v_add_f32_e32 v167, 0x41000000, v65
	v_cmp_gt_f32_e32 vcc, v166, v167
	s_cbranch_vccz .LBB0_950
	v_max_f32_e32 v166, v166, v166
	v_max_f32_e32 v167, v65, v65
	v_max_f32_e32 v167, v167, v166
	v_sub_f32_e32 v65, v65, v167
	v_exp_f32_e32 v166, v65
	v_mov_b32_e32 v65, v167
	v_pk_mul_f32 v[34:35], v[34:35], v[166:167] op_sel_hi:[1,0]
	v_pk_mul_f32 v[32:33], v[32:33], v[166:167] op_sel_hi:[1,0]
	v_pk_mul_f32 v[30:31], v[30:31], v[166:167] op_sel_hi:[1,0]
	v_pk_mul_f32 v[28:29], v[28:29], v[166:167] op_sel_hi:[1,0]
	v_pk_mul_f32 v[26:27], v[26:27], v[166:167] op_sel_hi:[1,0]
	v_pk_mul_f32 v[24:25], v[24:25], v[166:167] op_sel_hi:[1,0]
	v_pk_mul_f32 v[22:23], v[22:23], v[166:167] op_sel_hi:[1,0]
	v_pk_mul_f32 v[20:21], v[20:21], v[166:167] op_sel_hi:[1,0]
	v_pk_mul_f32 v[18:19], v[18:19], v[166:167] op_sel_hi:[1,0]
	v_pk_mul_f32 v[16:17], v[16:17], v[166:167] op_sel_hi:[1,0]
	v_pk_mul_f32 v[14:15], v[14:15], v[166:167] op_sel_hi:[1,0]
	v_pk_mul_f32 v[12:13], v[12:13], v[166:167] op_sel_hi:[1,0]
	v_pk_mul_f32 v[10:11], v[10:11], v[166:167] op_sel_hi:[1,0]
	v_pk_mul_f32 v[8:9], v[8:9], v[166:167] op_sel_hi:[1,0]
	v_pk_mul_f32 v[6:7], v[6:7], v[166:167] op_sel_hi:[1,0]
	v_pk_mul_f32 v[4:5], v[4:5], v[166:167] op_sel_hi:[1,0]
	v_mul_f32_e32 v3, v3, v166
	s_branch .LBB0_950

; #define LAS __attribute__((address_space(3)))
; __device__ __forceinline__ float xhalf_max(float m) { auto rr = __builtin_amdgcn_permlane32_swap(__float_as_uint(m), __float_as_uint(m), false, false); return fmaxf(__uint_as_float(rr[0]), __uint_as_float(rr[1])); }
; template <bool BAND, int OUTMODE>
; __device__ __forceinline__ void compute(LAS unsigned char* lds, const bf16x8 (&qr)[4], int tid, int mq0, int dil, int res, int kt_min, int bias_tab, float sink2,
;                                         bf16* ob, int opitch, float* lsep) {
;     ...
;             for (int i = 0; i < 16; ++i) S[i] = bl[32 * t + (i & 3) + 8 * (i >> 2)];
;         } else {
; #pragma unroll
;             for (int i = 0; i < 16; ++i) S[i] = 0.f;
;         }
; #pragma unroll
;         for (int s = 0; s < 4; ++s) { const bf16x8 kf = *(const LAS bf16x8*)(kb + t * 32 * KSTR + s * 32); S = __builtin_amdgcn_mfma_f32_32x32x16_bf16(kf, qr[s], S, 0, 0, 0); }
;         float m0 = fmaxf(fmaxf(S[0], S[1]), fmaxf(S[2], S[3])), m1 = fmaxf(fmaxf(S[4], S[5]), fmaxf(S[6], S[7])), m2 = fmaxf(fmaxf(S[8], S[9]), fmaxf(S[10], S[11])), m3 = fmaxf(fmaxf(S[12], S[13]), fmaxf(S[14], S[15]));
;         const float mt = xhalf_max(fmaxf(fmaxf(m0, m1), fmaxf(m2, m3)));
;         if (__any(mt > mref + THR)) {
;             const float mnew = fmaxf(mref, mt), f = __builtin_amdgcn_exp2f(mref - mnew);
;             mref = mnew; l *= f;
; #pragma unroll
;             for (int i = 0; i < 16; ++i) { o0[i] *= f; o1[i] *= f; }
;         }
.LBB0_961:
	v_add_u32_e32 v2, 0, v133
	v_add_u32_e32 v4, 0x1b000, v2
	v_add_u32_e32 v5, 0x1b008, v2
	v_add_u32_e32 v6, 0x1b020, v2
	v_add_u32_e32 v7, 0x1b028, v2
	ds_read2_b32 v[50:51], v4 offset1:1
	ds_read2_b32 v[52:53], v5 offset1:1
	ds_read2_b32 v[54:55], v6 offset1:1
	ds_read2_b32 v[56:57], v7 offset1:1
	v_add_u32_e32 v8, 0x1b040, v2
	v_add_u32_e32 v9, 0x1b048, v2
	v_add_u32_e32 v10, 0x1b060, v2
	v_add_u32_e32 v12, 0, v132
	v_add_u32_e32 v2, 0x1b068, v2
	ds_read_b128 v[4:7], v12
	ds_read2_b32 v[58:59], v8 offset1:1
	ds_read2_b32 v[60:61], v9 offset1:1
	ds_read2_b32 v[62:63], v10 offset1:1
	ds_read2_b32 v[64:65], v2 offset1:1
	ds_read_b128 v[8:11], v12 offset:32
	s_waitcnt vmcnt(17) lgkmcnt(1)
	v_mfma_f32_32x32x16_bf16 v[50:65], v[4:7], v[86:89], v[50:65]
	s_waitcnt vmcnt(16) lgkmcnt(0)
	v_mfma_f32_32x32x16_bf16 v[50:65], v[8:11], v[90:93], v[50:65]
	ds_read_b128 v[4:7], v12 offset:64
	ds_read_b128 v[8:11], v12 offset:96
	s_waitcnt vmcnt(15) lgkmcnt(1)
	v_mfma_f32_32x32x16_bf16 v[50:65], v[4:7], v[94:97], v[50:65]
	s_waitcnt vmcnt(14) lgkmcnt(0)
	v_mfma_f32_32x32x16_bf16 v[50:65], v[8:11], v[98:101], v[50:65]
	s_nop 11
	v_max3_f32 v2, v50, v51, v52
	v_max3_f32 v4, v53, v54, v55
	v_max3_f32 v5, v56, v57, v58
	v_max3_f32 v6, v59, v60, v61
	v_max3_f32 v7, v62, v63, v64
	v_max3_f32 v2, v2, v4, v65
	v_max3_f32 v5, v5, v6, v7
	v_max_f32_e32 v2, v2, v5
	v_mov_b32_e32 v4, v2
	s_nop 1
	v_permlane32_swap_b32_e32 v2, v4
	v_max_f32_e32 v2, v2, v4
	v_add_f32_e32 v4, 0x41000000, v130
	v_cmp_gt_f32_e32 vcc, v2, v4
	s_cbranch_vccz .LBB0_960
	v_max_f32_e32 v2, v2, v2
	v_max_f32_e32 v4, v130, v130
	v_max_f32_e32 v4, v4, v2
	v_sub_f32_e32 v2, v130, v4
	v_exp_f32_e32 v2, v2
	v_mov_b32_e32 v130, v4
	v_pk_mul_f32 v[48:49], v[48:49], v[2:3] op_sel_hi:[1,0]
	v_pk_mul_f32 v[46:47], v[46:47], v[2:3] op_sel_hi:[1,0]
	v_pk_mul_f32 v[44:45], v[44:45], v[2:3] op_sel_hi:[1,0]
	v_pk_mul_f32 v[42:43], v[42:43], v[2:3] op_sel_hi:[1,0]
	v_pk_mul_f32 v[40:41], v[40:41], v[2:3] op_sel_hi:[1,0]
	v_pk_mul_f32 v[38:39], v[38:39], v[2:3] op_sel_hi:[1,0]
	v_pk_mul_f32 v[36:37], v[36:37], v[2:3] op_sel_hi:[1,0]
	v_pk_mul_f32 v[34:35], v[34:35], v[2:3] op_sel_hi:[1,0]
	v_pk_mul_f32 v[32:33], v[32:33], v[2:3] op_sel_hi:[1,0]
	v_pk_mul_f32 v[30:31], v[30:31], v[2:3] op_sel_hi:[1,0]
	v_pk_mul_f32 v[28:29], v[28:29], v[2:3] op_sel_hi:[1,0]
	v_pk_mul_f32 v[26:27], v[26:27], v[2:3] op_sel_hi:[1,0]
	v_pk_mul_f32 v[24:25], v[24:25], v[2:3] op_sel_hi:[1,0]
	v_pk_mul_f32 v[22:23], v[22:23], v[2:3] op_sel_hi:[1,0]
	v_pk_mul_f32 v[20:21], v[20:21], v[2:3] op_sel_hi:[1,0]
	v_pk_mul_f32 v[18:19], v[18:19], v[2:3] op_sel_hi:[1,0]
	v_mul_f32_e32 v3, v3, v2
	s_branch .LBB0_960

; #define LAS __attribute__((address_space(3)))
; __device__ __forceinline__ float xhalf_max(float m) { auto rr = __builtin_amdgcn_permlane32_swap(__float_as_uint(m), __float_as_uint(m), false, false); return fmaxf(__uint_as_float(rr[0]), __uint_as_float(rr[1])); }
; template <bool BAND, int OUTMODE>
; __device__ __forceinline__ void compute(LAS unsigned char* lds, const bf16x8 (&qr)[4], int tid, int mq0, int dil, int res, int kt_min, int bias_tab, float sink2,
;                                         bf16* ob, int opitch, float* lsep) {
;     ...
;             for (int i = 0; i < 16; ++i) S[i] = 0.f;
;         }
; #pragma unroll
;         for (int s = 0; s < 4; ++s) { const bf16x8 kf = *(const LAS bf16x8*)(kb + t * 32 * KSTR + s * 32); S = __builtin_amdgcn_mfma_f32_32x32x16_bf16(kf, qr[s], S, 0, 0, 0); }
;         float m0 = fmaxf(fmaxf(S[0], S[1]), fmaxf(S[2], S[3])), m1 = fmaxf(fmaxf(S[4], S[5]), fmaxf(S[6], S[7])), m2 = fmaxf(fmaxf(S[8], S[9]), fmaxf(S[10], S[11])), m3 = fmaxf(fmaxf(S[12], S[13]), fmaxf(S[14], S[15]));
;         const float mt = xhalf_max(fmaxf(fmaxf(m0, m1), fmaxf(m2, m3)));
;         if (__any(mt > mref + THR)) {
;             const float mnew = fmaxf(mref, mt), f = __builtin_amdgcn_exp2f(mref - mnew);
;             mref = mnew; l *= f;
; #pragma unroll
;             for (int i = 0; i < 16; ++i) { o0[i] *= f; o1[i] *= f; }
;         }
.LBB0_969:
	v_add_u32_e32 v35, v52, v134
	ds_read_b128 v[36:39], v35
	ds_read_b128 v[54:57], v35 offset:32
	s_waitcnt vmcnt(5) lgkmcnt(1)
	v_mfma_f32_32x32x16_bf16 v[36:51], v[36:39], v[82:85], 0
	s_waitcnt lgkmcnt(0)
	v_mfma_f32_32x32x16_bf16 v[36:51], v[54:57], v[74:77], v[36:51]
	ds_read_b128 v[54:57], v35 offset:64
	ds_read_b128 v[58:61], v35 offset:96
	s_waitcnt lgkmcnt(1)
	v_mfma_f32_32x32x16_bf16 v[36:51], v[54:57], v[78:81], v[36:51]
	s_waitcnt vmcnt(4) lgkmcnt(0)
	v_mfma_f32_32x32x16_bf16 v[36:51], v[58:61], v[102:105], v[36:51]
	s_nop 11
	v_max3_f32 v35, v36, v37, v38
	v_max3_f32 v54, v39, v40, v41
	v_max3_f32 v55, v42, v43, v44
	v_max3_f32 v56, v45, v46, v47
	v_max3_f32 v57, v48, v49, v50
	v_max3_f32 v35, v35, v54, v51
	v_max3_f32 v55, v55, v56, v57
	v_max_f32_e32 v35, v35, v55
	v_mov_b32_e32 v54, v35
	s_nop 1
	v_permlane32_swap_b32_e32 v35, v54
	v_max_f32_e32 v35, v35, v54
	v_add_f32_e32 v54, 0x41000000, v53
	v_cmp_gt_f32_e32 vcc, v35, v54
	s_cbranch_vccz .LBB0_968
	v_max_f32_e32 v35, v35, v35
	v_max_f32_e32 v54, v53, v53
	v_max_f32_e32 v35, v54, v35
	v_sub_f32_e32 v53, v53, v35
	v_exp_f32_e32 v54, v53
	v_mov_b32_e32 v53, v35
	v_pk_mul_f32 v[32:33], v[32:33], v[54:55] op_sel_hi:[1,0]
	v_pk_mul_f32 v[30:31], v[30:31], v[54:55] op_sel_hi:[1,0]
	v_pk_mul_f32 v[28:29], v[28:29], v[54:55] op_sel_hi:[1,0]
	v_pk_mul_f32 v[26:27], v[26:27], v[54:55] op_sel_hi:[1,0]
	v_pk_mul_f32 v[24:25], v[24:25], v[54:55] op_sel_hi:[1,0]
	v_pk_mul_f32 v[22:23], v[22:23], v[54:55] op_sel_hi:[1,0]
	v_pk_mul_f32 v[20:21], v[20:21], v[54:55] op_sel_hi:[1,0]
	v_pk_mul_f32 v[18:19], v[18:19], v[54:55] op_sel_hi:[1,0]
	v_pk_mul_f32 v[16:17], v[16:17], v[54:55] op_sel_hi:[1,0]
	v_pk_mul_f32 v[14:15], v[14:15], v[54:55] op_sel_hi:[1,0]
	v_pk_mul_f32 v[12:13], v[12:13], v[54:55] op_sel_hi:[1,0]
	v_pk_mul_f32 v[10:11], v[10:11], v[54:55] op_sel_hi:[1,0]
	v_pk_mul_f32 v[8:9], v[8:9], v[54:55] op_sel_hi:[1,0]
	v_pk_mul_f32 v[6:7], v[6:7], v[54:55] op_sel_hi:[1,0]
	v_pk_mul_f32 v[4:5], v[4:5], v[54:55] op_sel_hi:[1,0]
	v_pk_mul_f32 v[2:3], v[2:3], v[54:55] op_sel_hi:[1,0]
	v_mul_f32_e32 v34, v34, v54
	s_branch .LBB0_968
